# indexer tile loop: one static s_setprio 1 for waves 4-7 (reset after the loop) so the two waves of a SIMD interleave their MFMA and VALU blocks
# speedup vs baseline: 1.0010x; 1.0010x over previous
.LBB0_404:
	s_lshl_b32 s12, s12, 10
	s_lshl_b32 s0, s13, 6
	s_add_i32 s1, s12, 0x400
	s_add_i32 s13, s0, 64
	s_min_u32 s1, s1, s13
	s_sub_i32 s1, s1, s12
	s_ashr_i32 s24, s1, 5
	s_cmp_lt_i32 s24, 1
	s_cbranch_scc1 .LBB0_407
	s_mul_i32 s13, s4, 0x3400000
	s_mul_hi_u32 s1, s4, 0x3400000
	s_add_u32 s14, s82, s13
	s_addc_u32 s15, s83, s1
	s_add_i32 s13, s0, s17
	v_or_b32_e32 v4, s13, v158
	v_mov_b64_e32 v[2:3], s[14:15]
	v_mad_u64_u32 v[4:5], s[0:1], v4, s18, v[2:3]
	s_or_b32 s25, s13, 2
	v_lshl_add_u64 v[4:5], v[4:5], 0, v[144:145]
	s_waitcnt vmcnt(30)
	v_or_b32_e32 v6, s25, v158
	v_lshl_add_u64 v[4:5], v[4:5], 0, v[148:149]
	v_mad_u64_u32 v[6:7], s[0:1], v6, s18, v[2:3]
	s_waitcnt vmcnt(22)
	v_lshl_add_u64 v[38:39], v[4:5], 0, s[6:7]
	v_add_co_u32_e32 v4, vcc, s19, v4
	v_lshl_add_u64 v[6:7], v[6:7], 0, v[144:145]
	s_nop 0
	v_addc_co_u32_e32 v5, vcc, 0, v5, vcc
	v_lshl_add_u64 v[6:7], v[6:7], 0, v[148:149]
	s_or_b32 s26, s13, 4
	global_load_dwordx4 v[66:69], v[38:39], off offset:64
	global_load_dwordx4 v[70:73], v[38:39], off offset:96
	v_lshl_add_u64 v[8:9], v[6:7], 0, s[6:7]
	global_load_dwordx4 v[74:77], v[4:5], off offset:2560
	global_load_dwordx4 v[78:81], v[8:9], off offset:32
	global_load_dwordx4 v[82:85], v[8:9], off offset:64
	global_load_dwordx4 v[86:89], v[8:9], off offset:96
	v_or_b32_e32 v4, s26, v158
	v_mad_u64_u32 v[4:5], s[0:1], v4, s18, v[2:3]
	v_add_co_u32_e32 v18, vcc, s19, v6
	v_lshl_add_u64 v[4:5], v[4:5], 0, v[144:145]
	s_nop 0
	v_addc_co_u32_e32 v19, vcc, 0, v7, vcc
	v_lshl_add_u64 v[4:5], v[4:5], 0, v[148:149]
	v_add_u32_e32 v6, s25, v142
	v_lshl_add_u64 v[20:21], v[4:5], 0, s[6:7]
	v_add_co_u32_e32 v4, vcc, s19, v4
	v_mad_i64_i32 v[22:23], s[0:1], v6, s18, v[2:3]
	v_add_u32_e32 v6, s13, v142
	v_addc_co_u32_e32 v5, vcc, 0, v5, vcc
	v_mad_i64_i32 v[10:11], s[0:1], v6, s18, v[2:3]
	v_add_co_u32_e32 v6, vcc, s20, v10
	s_or_b32 s25, s13, 6
	s_nop 0
	v_addc_co_u32_e32 v7, vcc, 0, v11, vcc
	v_or_b32_e32 v28, s25, v158
	v_add_co_u32_e32 v12, vcc, s20, v22
	v_mad_u64_u32 v[28:29], s[0:1], v28, s18, v[2:3]
	s_nop 0
	v_addc_co_u32_e32 v13, vcc, 0, v23, vcc
	v_lshl_add_u64 v[14:15], v[10:11], 0, s[10:11]
	v_lshl_add_u64 v[28:29], v[28:29], 0, v[144:145]
	global_load_dwordx4 v[6:9], v[6:7], off offset:640
	s_nop 0
	global_load_dwordx4 v[10:13], v[12:13], off offset:640
	s_nop 0
	global_load_dwordx4 v[14:17], v[14:15], off offset:16
	s_nop 0
	global_load_dwordx4 v[90:93], v[18:19], off offset:2560
	global_load_dwordx4 v[94:97], v[20:21], off offset:32
	global_load_dwordx4 v[98:101], v[20:21], off offset:64
	global_load_dwordx4 v[102:105], v[20:21], off offset:96
	v_add_u32_e32 v18, s26, v142
	v_lshl_add_u64 v[34:35], v[28:29], 0, v[148:149]
	v_add_u32_e32 v28, s25, v142
	v_mad_i64_i32 v[26:27], s[0:1], v18, s18, v[2:3]
	v_mad_i64_i32 v[2:3], s[0:1], v28, s18, v[2:3]
	v_add_co_u32_e32 v18, vcc, s20, v26
	v_add_co_u32_e64 v28, s[0:1], s20, v2
	s_nop 0
	v_addc_co_u32_e32 v19, vcc, 0, v27, vcc
	v_lshl_add_u64 v[22:23], v[22:23], 0, s[10:11]
	v_addc_co_u32_e64 v29, s[0:1], 0, v3, s[0:1]
	v_lshl_add_u64 v[30:31], v[26:27], 0, s[10:11]
	global_load_dwordx4 v[18:21], v[18:19], off offset:640
	s_nop 0
	global_load_dwordx4 v[22:25], v[22:23], off offset:16
	v_lshl_add_u64 v[36:37], v[34:35], 0, s[6:7]
	global_load_dwordx4 v[26:29], v[28:29], off offset:640
	s_nop 0
	global_load_dwordx4 v[30:33], v[30:31], off offset:16
	s_nop 0
	global_load_dwordx4 v[106:109], v[4:5], off offset:2560
	global_load_dwordx4 v[110:113], v[36:37], off offset:32
	global_load_dwordx4 v[114:117], v[36:37], off offset:64
	global_load_dwordx4 v[118:121], v[36:37], off offset:96
	v_or_b32_e32 v4, s12, v146
	v_mul_u32_u24_e32 v4, 0x1a00, v4
	v_mov_b32_e32 v5, v145
	v_add_co_u32_e32 v34, vcc, s19, v34
	v_lshl_add_u64 v[4:5], v[4:5], 1, s[14:15]
	s_nop 0
	v_addc_co_u32_e32 v35, vcc, 0, v35, vcc
	v_lshl_add_u64 v[4:5], v[4:5], 0, v[148:149]
	v_lshl_add_u64 v[2:3], v[2:3], 0, s[10:11]
	v_lshl_add_u64 v[152:153], v[4:5], 0, s[8:9]
	global_load_dwordx4 v[122:125], v[34:35], off offset:2560
	s_nop 0
	global_load_dwordx4 v[34:37], v[2:3], off offset:16
	global_load_dwordx4 v[126:129], v[38:39], off offset:32
	global_load_dwordx4 v[130:133], v[152:153], off offset:96
	global_load_dwordx4 v[134:137], v[152:153], off offset:64
	global_load_dwordx4 v[138:141], v[152:153], off offset:32
	v_add_co_u32_e32 v2, vcc, s20, v4
	s_lshl_b64 s[14:15], s[4:5], 12
	s_nop 0
	v_addc_co_u32_e32 v3, vcc, 0, v5, vcc
	global_load_dwordx4 v[2:5], v[2:3], off offset:512
	s_add_u32 s14, s13, s14
	s_addc_u32 s15, 0, s15
	v_lshl_add_u64 v[38:39], s[14:15], 0, v[142:143]
	v_lshlrev_b64 v[38:39], 14, v[38:39]
	s_mov_b32 s13, s5
	v_lshl_add_u64 v[38:39], s[84:85], 0, v[38:39]
	s_mov_b32 s0, 0
	v_lshl_add_u64 v[38:39], s[12:13], 2, v[38:39]
	v_mov_b32_e32 v151, v145
	v_lshl_add_u64 v[154:155], v[38:39], 0, v[150:151]
	s_mov_b32 s4, s0
	s_waitcnt vmcnt(20)
	v_lshlrev_b32_e32 v177, 16, v10
	s_waitcnt vmcnt(19)
	v_lshlrev_b32_e32 v168, 16, v14
	v_and_b32_e32 v169, 0xffff0000, v14
	v_lshlrev_b32_e32 v170, 16, v15
	v_lshlrev_b32_e32 v151, 16, v6
	v_and_b32_e32 v161, 0xffff0000, v6
	v_lshlrev_b32_e32 v162, 16, v7
	v_and_b32_e32 v163, 0xffff0000, v7
	v_lshlrev_b32_e32 v164, 16, v8
	v_and_b32_e32 v165, 0xffff0000, v8
	v_lshlrev_b32_e32 v166, 16, v9
	v_and_b32_e32 v167, 0xffff0000, v9
	v_and_b32_e32 v171, 0xffff0000, v15
	v_lshlrev_b32_e32 v172, 16, v16
	v_and_b32_e32 v173, 0xffff0000, v16
	v_lshlrev_b32_e32 v174, 16, v17
	v_and_b32_e32 v176, 0xffff0000, v17
	v_and_b32_e32 v178, 0xffff0000, v10
	v_lshlrev_b32_e32 v179, 16, v11
	v_and_b32_e32 v180, 0xffff0000, v11
	v_lshlrev_b32_e32 v181, 16, v12
	v_and_b32_e32 v182, 0xffff0000, v12
	v_lshlrev_b32_e32 v183, 16, v13
	v_and_b32_e32 v184, 0xffff0000, v13
	s_waitcnt vmcnt(13)
	v_lshlrev_b32_e32 v185, 16, v22
	v_and_b32_e32 v186, 0xffff0000, v22
	v_lshlrev_b32_e32 v187, 16, v23
	v_and_b32_e32 v188, 0xffff0000, v23
	v_lshlrev_b32_e32 v189, 16, v24
	v_and_b32_e32 v190, 0xffff0000, v24
	v_lshlrev_b32_e32 v191, 16, v25
	v_and_b32_e32 v192, 0xffff0000, v25
	v_lshlrev_b32_e32 v193, 16, v18
	v_and_b32_e32 v194, 0xffff0000, v18
	v_lshlrev_b32_e32 v195, 16, v19
	v_and_b32_e32 v196, 0xffff0000, v19
	v_lshlrev_b32_e32 v197, 16, v20
	v_and_b32_e32 v198, 0xffff0000, v20
	v_lshlrev_b32_e32 v199, 16, v21
	v_and_b32_e32 v200, 0xffff0000, v21
	s_waitcnt vmcnt(11)
	v_lshlrev_b32_e32 v201, 16, v30
	v_and_b32_e32 v202, 0xffff0000, v30
	v_lshlrev_b32_e32 v203, 16, v31
	v_and_b32_e32 v204, 0xffff0000, v31
	v_lshlrev_b32_e32 v205, 16, v32
	v_and_b32_e32 v206, 0xffff0000, v32
	v_lshlrev_b32_e32 v207, 16, v33
	v_and_b32_e32 v208, 0xffff0000, v33
	v_lshlrev_b32_e32 v209, 16, v26
	v_and_b32_e32 v210, 0xffff0000, v26
	v_lshlrev_b32_e32 v211, 16, v27
	v_and_b32_e32 v212, 0xffff0000, v27
	v_lshlrev_b32_e32 v213, 16, v28
	v_and_b32_e32 v214, 0xffff0000, v28
	v_lshlrev_b32_e32 v215, 16, v29
	v_and_b32_e32 v216, 0xffff0000, v29
	s_waitcnt vmcnt(5)
	v_lshlrev_b32_e32 v217, 16, v34
	v_and_b32_e32 v218, 0xffff0000, v34
	v_lshlrev_b32_e32 v219, 16, v35
	v_and_b32_e32 v220, 0xffff0000, v35
	v_lshlrev_b32_e32 v221, 16, v36
	v_and_b32_e32 v222, 0xffff0000, v36
	v_lshlrev_b32_e32 v223, 16, v37
	v_and_b32_e32 v224, 0xffff0000, v37
	s_cmp_ge_u32 s76, 4
	s_cbranch_scc0 .Lprio_idx
	s_setprio 1

.LBB0_407:
	s_setprio 0
	s_barrier
	s_and_saveexec_b64 s[0:1], s[2:3]
	s_cbranch_execz .LBB0_393
	s_mov_b64 s[14:15], exec
	v_mbcnt_lo_u32_b32 v2, s14, 0
	v_mbcnt_hi_u32_b32 v2, s15, v2
	v_cmp_eq_u32_e32 vcc, 0, v2
	s_and_saveexec_b64 s[12:13], vcc
	s_cbranch_execz .LBB0_392
	s_bcnt1_i32_b64 s4, s[14:15]
	v_mov_b32_e32 v3, s4
	global_atomic_add v3, v145, v3, s[54:55] offset:256 sc0
	s_branch .LBB0_392
